# up-projection K-loop: a unit's first two staging waits no longer wait for the previous unit's 16 epilogue stores (vmcnt 24)
# speedup vs baseline: 1.0125x; 1.0064x over previous
; #define PG8_STAGE(bufoff, gbase, voff) do { _Pragma("unroll") for (int _i = 0; _i < 2; ++_i) \
;         __builtin_amdgcn_global_load_lds((const unsigned*)((const char*)(gbase) + (voff)[_i]), (PG8_LAS unsigned*)(lds + (bufoff) + ldsw + _i * 8192), 16, 0, 0); } while (0)
; #define PG8_WAIT_V(n) asm volatile("s_waitcnt vmcnt(" #n ")" ::: "memory")
; #define PG8_BAR __builtin_amdgcn_s_barrier()
; template <class Epi, class Sched, bool ALIGN_EPI = false, bool SP2 = false>
; __device__ __forceinline__ void gemm_phase(PG8_LAS unsigned char* lds, const Gemm g, const Sched& S, const Epi& E, const int tid) {
;     ...
;     const char* cA = (const char*)g.A + (size_t)cur.pm * tstepA; const char* cB = (const char*)g.Bt + (size_t)cur.pn * tstep;
;     S.a_ready(cur);
;     if constexpr (SP2) {
;         PG8_STAGE(PG8_SB(0, 0), cB, voffB); PG8_STAGE(PG8_SB(0, 1), cB + hstep, voffB); PG8_STAGE(PG8_SA(0, 0), cA, voffA); PG8_STAGE(PG8_SA(0, 1), cA + hstepA, voffA);
;         if (wr == 1) PG8_BAR;
;         PG8_WAIT_V(2); PG8_BAR;
;         PG8_STAGE(PG8_SB(1, 0), cB + kstep, voffB); PG8_STAGE(PG8_SA(1, 0), cA + kstep, voffA); PG8_STAGE(PG8_SB(1, 1), cB + hstep + kstep, voffB);
;         PG8_WAIT_V(6); PG8_BAR;
.LBB0_51:
	v_lshl_add_u64 v[8:9], s[22:23], 0, v[0:1]
	v_mov_b32_e32 v135, v1
	s_add_i32 s42, s33, 0x18000
	v_lshl_add_u64 v[10:11], s[22:23], 0, v[134:135]
	v_mov_b32_e32 v131, v1
	s_and_b32 s1, s1, 3
	v_lshl_add_u64 v[8:9], v[8:9], 0, s[86:87]
	s_mov_b32 m0, s42
	s_add_i32 s43, s33, 0x1a000
	v_lshl_add_u64 v[12:13], s[24:25], 0, v[130:131]
	v_mov_b32_e32 v133, v1
	s_lshl_b32 s9, s10, 13
	s_lshl_b32 s11, s1, 12
	s_waitcnt vmcnt(2)
	s_barrier
	global_load_lds_dwordx4 v[8:9], off
	v_lshl_add_u64 v[8:9], v[10:11], 0, s[86:87]
	s_mov_b32 m0, s43
	s_add_i32 s44, s33, 0x8000
	s_add_i32 s45, s33, 0xa000
	v_lshl_add_u64 v[14:15], s[24:25], 0, v[132:133]
	global_load_lds_dwordx4 v[8:9], off
	v_lshl_add_u64 v[8:9], v[12:13], 0, s[86:87]
	s_mov_b32 m0, s44
	s_add_u32 s12, s22, 0x40080
	global_load_lds_dwordx4 v[8:9], off
	v_lshl_add_u64 v[8:9], v[14:15], 0, s[86:87]
	s_mov_b32 m0, s45
	s_addc_u32 s13, s23, 0
	s_add_i32 s46, s33, 0x1c000
	global_load_lds_dwordx4 v[8:9], off
	v_lshl_add_u64 v[8:9], s[12:13], 0, v[0:1]
	s_mov_b32 m0, s46
	s_add_i32 s47, s33, 0x1e000
	global_load_lds_dwordx4 v[8:9], off
	v_lshl_add_u64 v[8:9], s[12:13], 0, v[134:135]
	s_mov_b32 m0, s47
	s_cmpk_lt_u32 s8, 0x100
	global_load_lds_dwordx4 v[8:9], off
	v_and_b32_e32 v8, 15, v232
	v_and_b32_e32 v9, 48, v232
	v_lshlrev_b32_e32 v11, 2, v8
	v_lshl_or_b32 v10, v8, 6, v9
	v_and_b32_e32 v12, 32, v11
	v_lshlrev_b32_e32 v8, 11, v8
	s_sext_i32_i8 s51, s0
	v_bitop3_b32 v144, v10, s9, v12 bitop3:0xde
	s_cselect_b64 s[8:9], -1, 0
	s_lshl_b32 s0, s1, 6
	v_lshl_or_b32 v8, s10, 17, v8
	v_or3_b32 v146, s0, v8, v9
	v_lshlrev_b32_e32 v8, 14, v2
	v_and_b32_e32 v8, 0xffff8000, v8
	v_lshl_add_u32 v6, v6, 11, v8
	v_and_b32_e32 v2, 1, v2
	v_lshl_or_b32 v2, v2, 6, v6
	v_lshl_add_u32 v136, v7, 1, v2
	v_lshlrev_b32_e32 v2, 14, v3
	s_lshl_b32 s1, s10, 8
	v_and_b32_e32 v2, 0xffff8000, v2
	s_waitcnt vmcnt(6)
	s_add_i32 s1, s1, 0x20200
	v_lshl_add_u32 v2, v4, 11, v2
	v_and_b32_e32 v3, 1, v3
	v_bitop3_b32 v10, s11, v10, v12 bitop3:0xf6
	s_add_u32 s10, s74, 0x8000000
	v_lshl_or_b32 v2, v3, 6, v2
	v_or_b32_e32 v145, s1, v11
	s_addc_u32 s11, s75, 0
	v_mov_b32_e32 v137, v1
	v_lshl_add_u32 v138, v5, 1, v2
	v_mov_b32_e32 v139, v1
	s_mov_b32 s48, 0
	v_or_b32_e32 v147, 0x10000, v10
	v_add_u32_e32 v148, 0x10400, v10
	v_add_u32_e32 v149, 0x10800, v10
	v_add_u32_e32 v150, 0x10c00, v10
	v_or_b32_e32 v151, 0x14000, v10
	v_add_u32_e32 v152, 0x14400, v10
	v_add_u32_e32 v153, 0x14800, v10
	v_add_u32_e32 v154, 0x14c00, v10
	s_add_i32 s49, s33, 0xc000
	s_add_i32 s50, s33, 0xe000
	v_or_b32_e32 v155, 0x18000, v10
	v_add_u32_e32 v156, 0x18400, v10
	v_add_u32_e32 v157, 0x18800, v10
	v_add_u32_e32 v158, 0x18c00, v10
	v_or_b32_e32 v159, 0x1c000, v10
	v_add_u32_e32 v160, 0x1c400, v10
	v_add_u32_e32 v161, 0x1c800, v10
	v_add_u32_e32 v162, 0x1cc00, v10
	s_barrier
	s_mov_b32 s100, 0
	s_branch .LBB0_54

; #define PG8_STAGE(bufoff, gbase, voff) do { _Pragma("unroll") for (int _i = 0; _i < 2; ++_i) \
;         __builtin_amdgcn_global_load_lds((const unsigned*)((const char*)(gbase) + (voff)[_i]), (PG8_LAS unsigned*)(lds + (bufoff) + ldsw + _i * 8192), 16, 0, 0); } while (0)
; #define PG8_LDA(dst, b, h) do { _Pragma("unroll") for (int m = 0; m < 4; ++m) _Pragma("unroll") for (int k = 0; k < 2; ++k) dst[m][k] = *(const PG8_LAS bf16x8*)(lds + PG8_SA(b, h) + aoff + m * 2048 + k * 1024); } while (0)
; #define PG8_LDB(dst, b, h) do { _Pragma("unroll") for (int n = 0; n < 2; ++n) _Pragma("unroll") for (int k = 0; k < 2; ++k) dst[n][k] = *(const PG8_LAS bf16x8*)(lds + PG8_SB(b, h) + boff + n * 2048 + k * 1024); } while (0)
; #define PG8_MMA(ai, bj, At, Bt) do { __builtin_amdgcn_s_setprio(1); _Pragma("unroll") for (int m = 0; m < 4; ++m) _Pragma("unroll") for (int n = 0; n < 2; ++n) _Pragma("unroll") for (int k = 0; k < 2; ++k) \
;         acc[ai][bj][m][n] = __builtin_amdgcn_mfma_f32_16x16x32_bf16(Bt[n][k], At[m][k], acc[ai][bj][m][n], 0, 0, 0); __builtin_amdgcn_s_setprio(0); } while (0)
; #define PG8_WAIT_V(n) asm volatile("s_waitcnt vmcnt(" #n ")" ::: "memory")
; #define PG8_WAIT_L(n) asm volatile("s_waitcnt lgkmcnt(" #n ")" ::: "memory")
; #define PG8_BAR __builtin_amdgcn_s_barrier()
; #define PG8_SCHED __builtin_amdgcn_sched_barrier(0)
; template <class Epi, class Sched, bool ALIGN_EPI = false, bool SP2 = false>
; __device__ __forceinline__ void gemm_phase(PG8_LAS unsigned char* lds, const Gemm g, const Sched& S, const Epi& E, const int tid) {
;     ...
;             PG8_LDB(B0, 0, 0); PG8_LDB(B1, 0, 1); PG8_SCHED; PG8_LDA(At, 0, 0); PG8_STAGE(PG8_SA(1, 1), a1 + hstepA, voffA);
;             PG8_WAIT_V(8); PG8_WAIT_L(0); PG8_BAR; PG8_MMA(0, 0, At, B0); PG8_MMA(0, 1, At, B1); PG8_BAR; PG8_SCHED;
;             PG8_LDA(At, 0, 1); PG8_STAGE(PG8_SB(0, 0), b2, voffB); PG8_STAGE(PG8_SB(0, 1), b2 + hstep, voffB); PG8_STAGE(PG8_SA(0, 0), a2, voffA);
;             PG8_WAIT_V(8); PG8_WAIT_L(0); PG8_BAR; PG8_MMA(1, 0, At, B0); PG8_MMA(1, 1, At, B1); PG8_BAR; PG8_SCHED;
.LBB0_61:
	ds_read_b128 v[140:143], v147
	ds_read_b128 v[164:167], v148
	ds_read_b128 v[168:171], v149
	ds_read_b128 v[172:175], v150
	ds_read_b128 v[176:179], v151
	ds_read_b128 v[180:183], v152
	ds_read_b128 v[184:187], v153
	ds_read_b128 v[188:191], v154
	s_add_u32 s24, s22, 0xfffc0080
	s_addc_u32 s25, s23, -1
	s_cmp_eq_u32 s56, 12
	s_cselect_b32 s27, s15, s25
	s_cselect_b32 s26, s52, s24
	s_cselect_b32 s25, s13, s55
	s_cselect_b32 s24, s53, s54
	s_mov_b32 m0, s49
	v_lshl_add_u64 v[212:213], s[22:23], 0, v[138:139]
	ds_read_b128 v[196:199], v144
	ds_read_b128 v[200:203], v144 offset:1024
	ds_read_b128 v[204:207], v144 offset:2048
	ds_read_b128 v[208:211], v144 offset:3072
	ds_read_b128 v[218:221], v144 offset:4096
	ds_read_b128 v[234:237], v144 offset:5120
	ds_read_b128 v[240:243], v144 offset:6144
	ds_read_b128 v[244:247], v144 offset:7168
	global_load_lds_dwordx4 v[212:213], off
	v_lshl_add_u64 v[212:213], s[22:23], 0, v[136:137]
	s_mov_b32 m0, s50
	s_nop 0
	global_load_lds_dwordx4 v[212:213], off
	s_cmp_eq_u32 s100, 0
	s_cbranch_scc1 .Lup_w8_0
	s_add_i32 s100, s100, -1
	s_waitcnt vmcnt(24)
	s_branch .Lup_wd_0
.Lup_w8_0:
	s_waitcnt vmcnt(8)
.Lup_wd_0:
	s_waitcnt lgkmcnt(0)
	s_barrier
	s_setprio 1
	s_waitcnt lgkmcnt(0)
	v_mfma_f32_16x16x32_bf16 v[126:129], v[140:143], v[196:199], v[126:129]
	v_mfma_f32_16x16x32_bf16 v[122:125], v[168:171], v[196:199], v[122:125]
	v_mfma_f32_16x16x32_bf16 v[110:113], v[140:143], v[204:207], v[110:113]
	v_mfma_f32_16x16x32_bf16 v[106:109], v[168:171], v[204:207], v[106:109]
	v_mfma_f32_16x16x32_bf16 v[94:97], v[140:143], v[218:221], v[94:97]
	v_mfma_f32_16x16x32_bf16 v[90:93], v[168:171], v[218:221], v[90:93]
	v_mfma_f32_16x16x32_bf16 v[78:81], v[140:143], v[240:243], v[78:81]
	v_mfma_f32_16x16x32_bf16 v[74:77], v[168:171], v[240:243], v[74:77]
	v_mfma_f32_16x16x32_bf16 v[126:129], v[164:167], v[200:203], v[126:129]
	v_mfma_f32_16x16x32_bf16 v[122:125], v[172:175], v[200:203], v[122:125]
	v_mfma_f32_16x16x32_bf16 v[110:113], v[164:167], v[208:211], v[110:113]
	v_mfma_f32_16x16x32_bf16 v[106:109], v[172:175], v[208:211], v[106:109]
	v_mfma_f32_16x16x32_bf16 v[94:97], v[164:167], v[234:237], v[94:97]
	v_mfma_f32_16x16x32_bf16 v[90:93], v[172:175], v[234:237], v[90:93]
	v_mfma_f32_16x16x32_bf16 v[78:81], v[164:167], v[244:247], v[78:81]
	v_mfma_f32_16x16x32_bf16 v[74:77], v[172:175], v[244:247], v[74:77]
	s_setprio 0
	s_setprio 1
	v_mfma_f32_16x16x32_bf16 v[118:121], v[176:179], v[196:199], v[118:121]
	v_mfma_f32_16x16x32_bf16 v[114:117], v[184:187], v[196:199], v[114:117]
	v_mfma_f32_16x16x32_bf16 v[102:105], v[176:179], v[204:207], v[102:105]
	v_mfma_f32_16x16x32_bf16 v[98:101], v[184:187], v[204:207], v[98:101]
	v_mfma_f32_16x16x32_bf16 v[86:89], v[176:179], v[218:221], v[86:89]
	v_mfma_f32_16x16x32_bf16 v[82:85], v[184:187], v[218:221], v[82:85]
	v_mfma_f32_16x16x32_bf16 v[70:73], v[176:179], v[240:243], v[70:73]
	v_mfma_f32_16x16x32_bf16 v[66:69], v[184:187], v[240:243], v[66:69]
	v_mfma_f32_16x16x32_bf16 v[118:121], v[180:183], v[200:203], v[118:121]
	v_mfma_f32_16x16x32_bf16 v[114:117], v[188:191], v[200:203], v[114:117]
	v_mfma_f32_16x16x32_bf16 v[102:105], v[180:183], v[208:211], v[102:105]
	v_mfma_f32_16x16x32_bf16 v[98:101], v[188:191], v[208:211], v[98:101]
	v_mfma_f32_16x16x32_bf16 v[86:89], v[180:183], v[234:237], v[86:89]
	v_mfma_f32_16x16x32_bf16 v[82:85], v[188:191], v[234:237], v[82:85]
	v_mfma_f32_16x16x32_bf16 v[70:73], v[180:183], v[244:247], v[70:73]
	v_mfma_f32_16x16x32_bf16 v[66:69], v[188:191], v[244:247], v[66:69]
	s_setprio 0
	s_barrier
	s_mov_b32 m0, s21
	v_lshl_add_u64 v[212:213], s[24:25], 0, v[0:1]
	s_add_u32 s58, s24, 0x40000
	ds_read_b128 v[196:199], v144 offset:16384
	ds_read_b128 v[200:203], v144 offset:17408
	ds_read_b128 v[204:207], v144 offset:18432
	ds_read_b128 v[208:211], v144 offset:19456
	ds_read_b128 v[218:221], v144 offset:20480
	ds_read_b128 v[234:237], v144 offset:21504
	ds_read_b128 v[240:243], v144 offset:22528
	ds_read_b128 v[244:247], v144 offset:23552
	global_load_lds_dwordx4 v[212:213], off
	v_lshl_add_u64 v[222:223], s[24:25], 0, v[134:135]
	s_mov_b32 m0, s36
	s_addc_u32 s59, s25, 0
	global_load_lds_dwordx4 v[222:223], off
	v_lshl_add_u64 v[228:229], s[58:59], 0, v[0:1]
	s_mov_b32 m0, s37
	v_lshl_add_u64 v[248:249], s[26:27], 0, v[132:133]
	global_load_lds_dwordx4 v[228:229], off
	v_lshl_add_u64 v[228:229], s[58:59], 0, v[134:135]
	s_mov_b32 m0, s38
	s_nop 0
	global_load_lds_dwordx4 v[228:229], off
	v_lshl_add_u64 v[228:229], s[26:27], 0, v[130:131]
	s_mov_b32 m0, s33
	s_nop 0
	global_load_lds_dwordx4 v[228:229], off
	s_mov_b32 m0, s39
	s_nop 0
	global_load_lds_dwordx4 v[248:249], off
	s_cmp_eq_u32 s100, 0
	s_cbranch_scc1 .Lup_w8_1
	s_add_i32 s100, s100, -1
	s_waitcnt vmcnt(24)
	s_branch .Lup_wd_1

; #define PG8_STAGE(bufoff, gbase, voff) do { _Pragma("unroll") for (int _i = 0; _i < 2; ++_i) \
;         __builtin_amdgcn_global_load_lds((const unsigned*)((const char*)(gbase) + (voff)[_i]), (PG8_LAS unsigned*)(lds + (bufoff) + ldsw + _i * 8192), 16, 0, 0); } while (0)
; #define PG8_LDA(dst, b, h) do { _Pragma("unroll") for (int m = 0; m < 4; ++m) _Pragma("unroll") for (int k = 0; k < 2; ++k) dst[m][k] = *(const PG8_LAS bf16x8*)(lds + PG8_SA(b, h) + aoff + m * 2048 + k * 1024); } while (0)
; #define PG8_LDB(dst, b, h) do { _Pragma("unroll") for (int n = 0; n < 2; ++n) _Pragma("unroll") for (int k = 0; k < 2; ++k) dst[n][k] = *(const PG8_LAS bf16x8*)(lds + PG8_SB(b, h) + boff + n * 2048 + k * 1024); } while (0)
; #define PG8_MMA(ai, bj, At, Bt) do { __builtin_amdgcn_s_setprio(1); _Pragma("unroll") for (int m = 0; m < 4; ++m) _Pragma("unroll") for (int n = 0; n < 2; ++n) _Pragma("unroll") for (int k = 0; k < 2; ++k) \
;         acc[ai][bj][m][n] = __builtin_amdgcn_mfma_f32_16x16x32_bf16(Bt[n][k], At[m][k], acc[ai][bj][m][n], 0, 0, 0); __builtin_amdgcn_s_setprio(0); } while (0)
; #define PG8_WAIT_V(n) asm volatile("s_waitcnt vmcnt(" #n ")" ::: "memory")
; #define PG8_WAIT_L(n) asm volatile("s_waitcnt lgkmcnt(" #n ")" ::: "memory")
; #define PG8_BAR __builtin_amdgcn_s_barrier()
; #define PG8_SCHED __builtin_amdgcn_sched_barrier(0)
; template <class Epi, class Sched, bool ALIGN_EPI = false, bool SP2 = false>
; __device__ __forceinline__ void gemm_phase(PG8_LAS unsigned char* lds, const Gemm g, const Sched& S, const Epi& E, const int tid) {
;     ...
;             PG8_WAIT_V(8); PG8_WAIT_L(0); PG8_BAR; PG8_MMA(1, 0, At, B0); PG8_MMA(1, 1, At, B1); PG8_BAR; PG8_SCHED;
;             PG8_LDB(B0, 1, 0); PG8_LDB(B1, 1, 1); PG8_SCHED; PG8_LDA(At, 1, 0); PG8_STAGE(PG8_SA(0, 1), a2 + hstepA, voffA);
;             PG8_WAIT_V(8); PG8_WAIT_L(0); PG8_BAR; PG8_MMA(0, 0, At, B0); PG8_MMA(0, 1, At, B1); PG8_BAR; PG8_SCHED;
.Lup_wd_1:
	s_waitcnt lgkmcnt(0)
	s_barrier
	s_setprio 1
	s_waitcnt lgkmcnt(0)
	v_mfma_f32_16x16x32_bf16 v[62:65], v[140:143], v[196:199], v[62:65]
	v_mfma_f32_16x16x32_bf16 v[58:61], v[168:171], v[196:199], v[58:61]
	v_mfma_f32_16x16x32_bf16 v[46:49], v[140:143], v[204:207], v[46:49]
	v_mfma_f32_16x16x32_bf16 v[42:45], v[168:171], v[204:207], v[42:45]
	v_mfma_f32_16x16x32_bf16 v[30:33], v[140:143], v[218:221], v[30:33]
	v_mfma_f32_16x16x32_bf16 v[26:29], v[168:171], v[218:221], v[26:29]
	v_mfma_f32_16x16x32_bf16 v[14:17], v[140:143], v[240:243], v[14:17]
	v_mfma_f32_16x16x32_bf16 v[10:13], v[168:171], v[240:243], v[10:13]
	v_mfma_f32_16x16x32_bf16 v[62:65], v[164:167], v[200:203], v[62:65]
	v_mfma_f32_16x16x32_bf16 v[58:61], v[172:175], v[200:203], v[58:61]
	v_mfma_f32_16x16x32_bf16 v[46:49], v[164:167], v[208:211], v[46:49]
	v_mfma_f32_16x16x32_bf16 v[42:45], v[172:175], v[208:211], v[42:45]
	v_mfma_f32_16x16x32_bf16 v[30:33], v[164:167], v[234:237], v[30:33]
	v_mfma_f32_16x16x32_bf16 v[26:29], v[172:175], v[234:237], v[26:29]
	v_mfma_f32_16x16x32_bf16 v[14:17], v[164:167], v[244:247], v[14:17]
	v_mfma_f32_16x16x32_bf16 v[10:13], v[172:175], v[244:247], v[10:13]
	s_setprio 0
	s_setprio 1
	v_mfma_f32_16x16x32_bf16 v[54:57], v[176:179], v[196:199], v[54:57]
	v_mfma_f32_16x16x32_bf16 v[50:53], v[184:187], v[196:199], v[50:53]
	v_mfma_f32_16x16x32_bf16 v[38:41], v[176:179], v[204:207], v[38:41]
	v_mfma_f32_16x16x32_bf16 v[34:37], v[184:187], v[204:207], v[34:37]
	v_mfma_f32_16x16x32_bf16 v[22:25], v[176:179], v[218:221], v[22:25]
	v_mfma_f32_16x16x32_bf16 v[18:21], v[184:187], v[218:221], v[18:21]
	v_mfma_f32_16x16x32_bf16 v[6:9], v[176:179], v[240:243], v[6:9]
	v_mfma_f32_16x16x32_bf16 v[2:5], v[184:187], v[240:243], v[2:5]
	v_mfma_f32_16x16x32_bf16 v[54:57], v[180:183], v[200:203], v[54:57]
	v_mfma_f32_16x16x32_bf16 v[50:53], v[188:191], v[200:203], v[50:53]
	v_mfma_f32_16x16x32_bf16 v[38:41], v[180:183], v[208:211], v[38:41]
	v_mfma_f32_16x16x32_bf16 v[34:37], v[188:191], v[208:211], v[34:37]
	v_mfma_f32_16x16x32_bf16 v[22:25], v[180:183], v[234:237], v[22:25]
	v_mfma_f32_16x16x32_bf16 v[18:21], v[188:191], v[234:237], v[18:21]
	v_mfma_f32_16x16x32_bf16 v[6:9], v[180:183], v[244:247], v[6:9]
	v_mfma_f32_16x16x32_bf16 v[2:5], v[188:191], v[244:247], v[2:5]
	s_setprio 0
	s_barrier
	ds_read_b128 v[140:143], v155
	ds_read_b128 v[164:167], v156
	ds_read_b128 v[168:171], v157
	ds_read_b128 v[172:175], v158
	ds_read_b128 v[176:179], v159
	ds_read_b128 v[180:183], v160
	ds_read_b128 v[184:187], v161
	ds_read_b128 v[188:191], v162
	s_add_u32 s26, s26, 0x40000
	s_addc_u32 s27, s27, 0
	s_mov_b32 m0, s40
	v_lshl_add_u64 v[250:251], s[26:27], 0, v[130:131]
	ds_read_b128 v[196:199], v144 offset:32768
	ds_read_b128 v[200:203], v144 offset:33792
	ds_read_b128 v[204:207], v144 offset:34816
	ds_read_b128 v[208:211], v144 offset:35840
	ds_read_b128 v[218:221], v144 offset:36864
	ds_read_b128 v[234:237], v144 offset:37888
	ds_read_b128 v[240:243], v144 offset:38912
	ds_read_b128 v[244:247], v144 offset:39936
	global_load_lds_dwordx4 v[250:251], off
	v_lshl_add_u64 v[250:251], s[26:27], 0, v[132:133]
	s_mov_b32 m0, s41
	s_nop 0
	global_load_lds_dwordx4 v[250:251], off
	s_waitcnt vmcnt(8)
	s_waitcnt lgkmcnt(0)
	s_barrier
	s_setprio 1
	s_waitcnt lgkmcnt(0)
	v_mfma_f32_16x16x32_bf16 v[126:129], v[140:143], v[196:199], v[126:129]
	v_mfma_f32_16x16x32_bf16 v[122:125], v[168:171], v[196:199], v[122:125]
	v_mfma_f32_16x16x32_bf16 v[110:113], v[140:143], v[204:207], v[110:113]
	v_mfma_f32_16x16x32_bf16 v[106:109], v[168:171], v[204:207], v[106:109]
	v_mfma_f32_16x16x32_bf16 v[94:97], v[140:143], v[218:221], v[94:97]
	v_mfma_f32_16x16x32_bf16 v[90:93], v[168:171], v[218:221], v[90:93]
	v_mfma_f32_16x16x32_bf16 v[78:81], v[140:143], v[240:243], v[78:81]
	v_mfma_f32_16x16x32_bf16 v[74:77], v[168:171], v[240:243], v[74:77]
	v_mfma_f32_16x16x32_bf16 v[126:129], v[164:167], v[200:203], v[126:129]
	v_mfma_f32_16x16x32_bf16 v[122:125], v[172:175], v[200:203], v[122:125]
	v_mfma_f32_16x16x32_bf16 v[110:113], v[164:167], v[208:211], v[110:113]
	v_mfma_f32_16x16x32_bf16 v[106:109], v[172:175], v[208:211], v[106:109]
	v_mfma_f32_16x16x32_bf16 v[94:97], v[164:167], v[234:237], v[94:97]
	v_mfma_f32_16x16x32_bf16 v[90:93], v[172:175], v[234:237], v[90:93]
	v_mfma_f32_16x16x32_bf16 v[78:81], v[164:167], v[244:247], v[78:81]
	v_mfma_f32_16x16x32_bf16 v[74:77], v[172:175], v[244:247], v[74:77]
	s_setprio 0
	s_setprio 1
	v_mfma_f32_16x16x32_bf16 v[118:121], v[176:179], v[196:199], v[118:121]
	v_mfma_f32_16x16x32_bf16 v[114:117], v[184:187], v[196:199], v[114:117]
	v_mfma_f32_16x16x32_bf16 v[102:105], v[176:179], v[204:207], v[102:105]
	v_mfma_f32_16x16x32_bf16 v[98:101], v[184:187], v[204:207], v[98:101]
	v_mfma_f32_16x16x32_bf16 v[86:89], v[176:179], v[218:221], v[86:89]
	v_mfma_f32_16x16x32_bf16 v[82:85], v[184:187], v[218:221], v[82:85]
	v_mfma_f32_16x16x32_bf16 v[70:73], v[176:179], v[240:243], v[70:73]
	v_mfma_f32_16x16x32_bf16 v[66:69], v[184:187], v[240:243], v[66:69]
	v_mfma_f32_16x16x32_bf16 v[118:121], v[180:183], v[200:203], v[118:121]
	v_mfma_f32_16x16x32_bf16 v[114:117], v[188:191], v[200:203], v[114:117]
	v_mfma_f32_16x16x32_bf16 v[102:105], v[180:183], v[208:211], v[102:105]
	v_mfma_f32_16x16x32_bf16 v[98:101], v[188:191], v[208:211], v[98:101]
	v_mfma_f32_16x16x32_bf16 v[86:89], v[180:183], v[234:237], v[86:89]
	v_mfma_f32_16x16x32_bf16 v[82:85], v[188:191], v[234:237], v[82:85]
	v_mfma_f32_16x16x32_bf16 v[70:73], v[180:183], v[244:247], v[70:73]
	v_mfma_f32_16x16x32_bf16 v[66:69], v[188:191], v[244:247], v[66:69]
	s_setprio 0
	s_barrier
; #define PG8_LAS __attribute__((address_space(3)))
; #define PG8_GAS __attribute__((address_space(1)))
; #define PG8_PACK8(y0, y1) (u32x4){cvt_pk_bf16((y0)[0], (y0)[1]), cvt_pk_bf16((y0)[2], (y0)[3]), cvt_pk_bf16((y1)[0], (y1)[1]), cvt_pk_bf16((y1)[2], (y1)[3])}
; #define PG8_LDA(dst, b, h) do { _Pragma("unroll") for (int m = 0; m < 4; ++m) _Pragma("unroll") for (int k = 0; k < 2; ++k) dst[m][k] = *(const PG8_LAS bf16x8*)(lds + PG8_SA(b, h) + aoff + m * 2048 + k * 1024); } while (0)
;     __device__ __forceinline__ void operator()(const f32x4 (&acc)[2][2][4][2], const Unit& u, int ui, int wr, int wc, int fr, int fq) const {
;     ...
;         const unsigned row0 = (unsigned)(u.pm * BM + wr * 64 + fr), colp = (unsigned)((u.pn & 3) * BM + wc * 32 + 8 * fq);
;         const PG8_LAS float* rsp = tab + (u.pm == pmA ? 0 : 256) + wr * 64 + fr;
;         float rsv[2][4];
; #pragma unroll
;         for (int ai = 0; ai < 2; ++ai)
; #pragma unroll
;             for (int m = 0; m < 4; ++m) rsv[ai][m] = rsp[ai * HALF + m * 16];
; #pragma unroll
;         for (int ai = 0; ai < 2; ++ai)
; #pragma unroll
;             for (int m = 0; m < 4; ++m) {
;                 const unsigned row = row0 + ai * HALF + m * 16; const float rs = rsv[ai][m];
; #pragma unroll
;                 for (int bj = 0; bj < 2; ++bj) {
;                     f32x4 y0 = acc[ai][bj][m][0] * rs, y1 = acc[ai][bj][m][1] * rs;
; #pragma unroll
;                     for (int e = 0; e < 4; ++e) { const float a = fmaxf(y0[e], 0.f), b = fmaxf(y1[e], 0.f); y0[e] = a * a; y1[e] = b * b; }
;                     const u32x4 hw = PG8_PACK8(y0, y1);
;     ...
;                     if (probe_mode == 1) { asm volatile("" :: "v"(hw)); } else
;     ...
;                     *(PG8_GAS u32x4*)((PG8_GAS unsigned char*)ws + E_QKVO + (size_t)((unsigned)(u.pm >> 4) * (24u << 20) + (unsigned)(u.pn >> 2) * (8u << 20) + row * 2048u + (colp + bj * HALF) * 2u)) = hw;
; template <class Epi, class Sched, bool ALIGN_EPI = false, bool SP2 = false>
; __device__ __forceinline__ void gemm_phase(PG8_LAS unsigned char* lds, const Gemm g, const Sched& S, const Epi& E, const int tid) {
;     ...
;             PG8_LDA(At, 1, 1); PG8_STAGE(PG8_SB(1, 0), b3, voffB); PG8_STAGE(PG8_SB(1, 1), b3 + hstep, voffB); PG8_STAGE(PG8_SA(1, 0), a3, voffA);
;             PG8_WAIT_V(8); PG8_WAIT_L(0); PG8_BAR; PG8_MMA(1, 0, At, B0); PG8_MMA(1, 1, At, B1); PG8_BAR; PG8_SCHED;
	s_mov_b32 m0, s42
	v_lshl_add_u64 v[212:213], v[212:213], 0, s[86:87]
	s_add_u32 s24, s24, 0x40080
	ds_read_b128 v[196:199], v144 offset:49152
	ds_read_b128 v[200:203], v144 offset:50176
	ds_read_b128 v[204:207], v144 offset:51200
	ds_read_b128 v[208:211], v144 offset:52224
	ds_read_b128 v[218:221], v144 offset:53248
	ds_read_b128 v[234:237], v144 offset:54272
	ds_read_b128 v[240:243], v144 offset:55296
	ds_read_b128 v[244:247], v144 offset:56320
	global_load_lds_dwordx4 v[212:213], off
	v_lshl_add_u64 v[212:213], v[222:223], 0, s[86:87]
	s_mov_b32 m0, s43
	s_addc_u32 s25, s25, 0
	global_load_lds_dwordx4 v[212:213], off
	v_lshl_add_u64 v[212:213], s[24:25], 0, v[0:1]
	s_mov_b32 m0, s46
	s_nop 0
	global_load_lds_dwordx4 v[212:213], off
	v_lshl_add_u64 v[212:213], s[24:25], 0, v[134:135]
	s_mov_b32 m0, s47
	s_nop 0
	global_load_lds_dwordx4 v[212:213], off
	v_lshl_add_u64 v[212:213], v[228:229], 0, s[86:87]
	s_mov_b32 m0, s44
	s_nop 0
	global_load_lds_dwordx4 v[212:213], off
	v_lshl_add_u64 v[212:213], v[248:249], 0, s[86:87]
	s_mov_b32 m0, s45
	s_nop 0
	global_load_lds_dwordx4 v[212:213], off
	s_waitcnt vmcnt(8)
	s_waitcnt lgkmcnt(0)
	s_barrier
	s_setprio 1
	s_waitcnt lgkmcnt(0)
	v_mfma_f32_16x16x32_bf16 v[62:65], v[140:143], v[196:199], v[62:65]
	v_mfma_f32_16x16x32_bf16 v[58:61], v[168:171], v[196:199], v[58:61]
	v_mfma_f32_16x16x32_bf16 v[46:49], v[140:143], v[204:207], v[46:49]
	v_mfma_f32_16x16x32_bf16 v[42:45], v[168:171], v[204:207], v[42:45]
	v_mfma_f32_16x16x32_bf16 v[30:33], v[140:143], v[218:221], v[30:33]
	v_mfma_f32_16x16x32_bf16 v[26:29], v[168:171], v[218:221], v[26:29]
	v_mfma_f32_16x16x32_bf16 v[14:17], v[140:143], v[240:243], v[14:17]
	v_mfma_f32_16x16x32_bf16 v[10:13], v[168:171], v[240:243], v[10:13]
	v_mfma_f32_16x16x32_bf16 v[62:65], v[164:167], v[200:203], v[62:65]
	v_mfma_f32_16x16x32_bf16 v[58:61], v[172:175], v[200:203], v[58:61]
	v_mfma_f32_16x16x32_bf16 v[46:49], v[164:167], v[208:211], v[46:49]
	v_mfma_f32_16x16x32_bf16 v[42:45], v[172:175], v[208:211], v[42:45]
	v_mfma_f32_16x16x32_bf16 v[30:33], v[164:167], v[234:237], v[30:33]
	v_mfma_f32_16x16x32_bf16 v[26:29], v[172:175], v[234:237], v[26:29]
	v_mfma_f32_16x16x32_bf16 v[14:17], v[164:167], v[244:247], v[14:17]
	v_mfma_f32_16x16x32_bf16 v[10:13], v[172:175], v[244:247], v[10:13]
	s_setprio 0
	s_setprio 1
	v_mfma_f32_16x16x32_bf16 v[54:57], v[176:179], v[196:199], v[54:57]
	v_mfma_f32_16x16x32_bf16 v[50:53], v[184:187], v[196:199], v[50:53]
	v_mfma_f32_16x16x32_bf16 v[38:41], v[176:179], v[204:207], v[38:41]
	v_mfma_f32_16x16x32_bf16 v[34:37], v[184:187], v[204:207], v[34:37]
	v_mfma_f32_16x16x32_bf16 v[22:25], v[176:179], v[218:221], v[22:25]
	v_mfma_f32_16x16x32_bf16 v[18:21], v[184:187], v[218:221], v[18:21]
	v_mfma_f32_16x16x32_bf16 v[6:9], v[176:179], v[240:243], v[6:9]
	v_mfma_f32_16x16x32_bf16 v[2:5], v[184:187], v[240:243], v[2:5]
	v_mfma_f32_16x16x32_bf16 v[54:57], v[180:183], v[200:203], v[54:57]
	v_mfma_f32_16x16x32_bf16 v[50:53], v[188:191], v[200:203], v[50:53]
	v_mfma_f32_16x16x32_bf16 v[38:41], v[180:183], v[208:211], v[38:41]
	v_mfma_f32_16x16x32_bf16 v[34:37], v[188:191], v[208:211], v[34:37]
	v_mfma_f32_16x16x32_bf16 v[22:25], v[180:183], v[234:237], v[22:25]
	v_mfma_f32_16x16x32_bf16 v[18:21], v[188:191], v[234:237], v[18:21]
	v_mfma_f32_16x16x32_bf16 v[6:9], v[180:183], v[244:247], v[6:9]
	v_mfma_f32_16x16x32_bf16 v[2:5], v[188:191], v[244:247], v[2:5]
	s_setprio 0
	s_barrier
	s_add_i32 s56, s56, 2
	s_add_u32 s54, s54, 0x100
	s_addc_u32 s55, s55, 0
	s_add_u32 s22, s22, 0x100
	s_addc_u32 s23, s23, 0
	s_cmp_gt_u32 s56, 13
	s_cbranch_scc0 .LBB0_61
	s_and_b64 vcc, exec, s[8:9]
	s_cbranch_vccz .LBB0_64
	s_barrier
.LBB0_64:
	s_lshl_b32 s13, s51, 9
	s_cmp_eq_u32 s20, s29
	s_cselect_b32 s15, 0, 0x400
	v_add_u32_e32 v140, s15, v145
	ds_read2_b32 v[164:165], v140 offset1:16
	ds_read2_b32 v[166:167], v140 offset0:32 offset1:48
	ds_read2_b32 v[142:143], v140 offset0:128 offset1:144
	ds_read2_b32 v[140:141], v140 offset0:160 offset1:176
	s_lshl_b32 s22, s51, 21
	s_lshr_b32 s15, s20, 4
	s_and_b32 s22, s22, 0xff800000
	s_lshl_b32 s20, s20, 19
	s_waitcnt lgkmcnt(0)
	v_pk_mul_f32 v[122:123], v[122:123], v[164:165] op_sel_hi:[1,0]
	s_add_i32 s22, s22, s20
	v_pk_mul_f32 v[126:127], v[126:127], v[164:165] op_sel_hi:[1,0]
	v_pk_mul_f32 v[124:125], v[124:125], v[164:165] op_sel_hi:[1,0]
	v_max_f32_e32 v122, 0, v122
	s_and_b32 s13, s13, 0x600
	v_add_u32_e32 v163, s22, v146
	v_pk_mul_f32 v[128:129], v[128:129], v[164:165] op_sel_hi:[1,0]
	v_mul_f32_e32 v168, v122, v122
	v_max_f32_e32 v122, 0, v127
	v_max_f32_e32 v123, 0, v123
	v_max_f32_e32 v124, 0, v124
	s_mul_i32 s15, s15, 0x1800000
	v_or_b32_e32 v163, s13, v163
	v_max_f32_e32 v126, 0, v126
	v_mul_f32_e32 v122, v122, v122
	v_mul_f32_e32 v127, v123, v123
	v_max_f32_e32 v123, 0, v128
	v_mul_f32_e32 v128, v124, v124
	v_max_f32_e32 v124, 0, v129
	v_max_f32_e32 v125, 0, v125
	v_pk_mul_f32 v[114:115], v[114:115], v[164:165] op_sel_hi:[1,0]
	v_add_u32_e32 v163, s15, v163
	v_mul_f32_e32 v126, v126, v126
	v_mul_f32_e32 v123, v123, v123
	v_mul_f32_e32 v124, v124, v124
	v_mul_f32_e32 v125, v125, v125
	v_cvt_pk_bf16_f32 v122, v126, v122
	v_pk_mul_f32 v[120:121], v[120:121], v[164:165] op_sel_hi:[1,0]
	v_pk_mul_f32 v[118:119], v[118:119], v[164:165] op_sel_hi:[1,0]
	v_pk_mul_f32 v[116:117], v[116:117], v[164:165] op_sel_hi:[1,0]
	v_max_f32_e32 v114, 0, v114
	v_max_f32_e32 v115, 0, v115
	v_cvt_pk_bf16_f32 v123, v123, v124
	v_cvt_pk_bf16_f32 v124, v168, v127
	v_cvt_pk_bf16_f32 v125, v128, v125
	global_store_dwordx4 v163, v[122:125], s[10:11] nt
	v_max_f32_e32 v118, 0, v118
	v_max_f32_e32 v116, 0, v116
	v_mul_f32_e32 v122, v114, v114
; #define PG8_GAS __attribute__((address_space(1)))
; #define PG8_PACK8(y0, y1) (u32x4){cvt_pk_bf16((y0)[0], (y0)[1]), cvt_pk_bf16((y0)[2], (y0)[3]), cvt_pk_bf16((y1)[0], (y1)[1]), cvt_pk_bf16((y1)[2], (y1)[3])}
;     __device__ __forceinline__ void operator()(const f32x4 (&acc)[2][2][4][2], const Unit& u, int ui, int wr, int wc, int fr, int fq) const {
;     ...
;         for (int ai = 0; ai < 2; ++ai)
; #pragma unroll
;             for (int m = 0; m < 4; ++m) {
;                 const unsigned row = row0 + ai * HALF + m * 16; const float rs = rsv[ai][m];
; #pragma unroll
;                 for (int bj = 0; bj < 2; ++bj) {
;                     f32x4 y0 = acc[ai][bj][m][0] * rs, y1 = acc[ai][bj][m][1] * rs;
; #pragma unroll
;                     for (int e = 0; e < 4; ++e) { const float a = fmaxf(y0[e], 0.f), b = fmaxf(y1[e], 0.f); y0[e] = a * a; y1[e] = b * b; }
;                     const u32x4 hw = PG8_PACK8(y0, y1);
;     ...
;                     if (probe_mode == 1) { asm volatile("" :: "v"(hw)); } else
;     ...
;                     *(PG8_GAS u32x4*)((PG8_GAS unsigned char*)ws + E_QKVO + (size_t)((unsigned)(u.pm >> 4) * (24u << 20) + (unsigned)(u.pn >> 2) * (8u << 20) + row * 2048u + (colp + bj * HALF) * 2u)) = hw;
	v_max_f32_e32 v114, 0, v119
	v_mul_f32_e32 v119, v115, v115
	v_max_f32_e32 v115, 0, v120
	v_mul_f32_e32 v118, v118, v118
	v_mul_f32_e32 v114, v114, v114
	v_mul_f32_e32 v115, v115, v115
	v_mul_f32_e32 v120, v116, v116
	v_max_f32_e32 v116, 0, v121
	v_max_f32_e32 v117, 0, v117
	v_mul_f32_e32 v116, v116, v116
	v_mul_f32_e32 v117, v117, v117
	v_cvt_pk_bf16_f32 v114, v118, v114
	v_cvt_pk_bf16_f32 v115, v115, v116
	v_or_b32_e32 v118, 0x100, v163
	v_cvt_pk_bf16_f32 v116, v122, v119
	v_cvt_pk_bf16_f32 v117, v120, v117
	global_store_dwordx4 v118, v[114:117], s[10:11] nt
	v_pk_mul_f32 v[90:91], v[90:91], v[166:167] op_sel_hi:[1,0]
	v_pk_mul_f32 v[94:95], v[94:95], v[166:167] op_sel_hi:[1,0]
	v_or_b32_e32 v115, 0x8000, v163
	v_mov_b32_e32 v114, v165
	v_pk_mul_f32 v[106:107], v[106:107], v[114:115] op_sel_hi:[1,0]
	v_pk_mul_f32 v[110:111], v[110:111], v[114:115] op_sel_hi:[1,0]
	v_pk_mul_f32 v[108:109], v[108:109], v[114:115] op_sel_hi:[1,0]
	v_max_f32_e32 v106, 0, v106
	v_pk_mul_f32 v[112:113], v[112:113], v[114:115] op_sel_hi:[1,0]
	v_mul_f32_e32 v116, v106, v106
	v_max_f32_e32 v106, 0, v111
	v_max_f32_e32 v107, 0, v107
	v_max_f32_e32 v108, 0, v108
	v_max_f32_e32 v110, 0, v110
	v_mul_f32_e32 v106, v106, v106
	v_mul_f32_e32 v111, v107, v107
	v_max_f32_e32 v107, 0, v112
	v_mul_f32_e32 v112, v108, v108
	v_max_f32_e32 v108, 0, v113
	v_max_f32_e32 v109, 0, v109
	v_pk_mul_f32 v[98:99], v[98:99], v[114:115] op_sel_hi:[1,0]
	v_mul_f32_e32 v110, v110, v110
	v_mul_f32_e32 v107, v107, v107
	v_mul_f32_e32 v108, v108, v108
	v_mul_f32_e32 v109, v109, v109
	v_cvt_pk_bf16_f32 v106, v110, v106
	v_pk_mul_f32 v[104:105], v[104:105], v[114:115] op_sel_hi:[1,0]
	v_pk_mul_f32 v[102:103], v[102:103], v[114:115] op_sel_hi:[1,0]
	v_pk_mul_f32 v[100:101], v[100:101], v[114:115] op_sel_hi:[1,0]
	v_max_f32_e32 v98, 0, v98
	v_max_f32_e32 v99, 0, v99
	v_cvt_pk_bf16_f32 v107, v107, v108
	v_cvt_pk_bf16_f32 v108, v116, v111
	v_cvt_pk_bf16_f32 v109, v112, v109
	global_store_dwordx4 v115, v[106:109], s[10:11] nt
	v_max_f32_e32 v102, 0, v102
	v_max_f32_e32 v100, 0, v100
	v_mul_f32_e32 v106, v98, v98
	v_max_f32_e32 v98, 0, v103
	v_mul_f32_e32 v103, v99, v99
	v_max_f32_e32 v99, 0, v104
	v_mul_f32_e32 v102, v102, v102
	v_mul_f32_e32 v98, v98, v98
	v_mul_f32_e32 v99, v99, v99
	v_mul_f32_e32 v104, v100, v100
	v_max_f32_e32 v100, 0, v105
	v_max_f32_e32 v101, 0, v101
	v_mul_f32_e32 v100, v100, v100
	v_mul_f32_e32 v101, v101, v101
	v_cvt_pk_bf16_f32 v98, v102, v98
	v_cvt_pk_bf16_f32 v99, v99, v100
	v_or_b32_e32 v102, 0x8100, v163
	v_pk_mul_f32 v[92:93], v[92:93], v[166:167] op_sel_hi:[1,0]
	v_max_f32_e32 v90, 0, v90
	v_cvt_pk_bf16_f32 v100, v106, v103
	v_cvt_pk_bf16_f32 v101, v104, v101
	global_store_dwordx4 v102, v[98:101], s[10:11] nt
	v_pk_mul_f32 v[96:97], v[96:97], v[166:167] op_sel_hi:[1,0]
	v_max_f32_e32 v91, 0, v91
	v_mul_f32_e32 v99, v90, v90
	v_max_f32_e32 v90, 0, v95
	v_max_f32_e32 v92, 0, v92
	v_max_f32_e32 v94, 0, v94
	v_mul_f32_e32 v90, v90, v90
	v_mul_f32_e32 v95, v91, v91
	v_max_f32_e32 v91, 0, v96
	v_mul_f32_e32 v96, v92, v92
	v_max_f32_e32 v92, 0, v97
	v_max_f32_e32 v93, 0, v93
	v_pk_mul_f32 v[82:83], v[82:83], v[166:167] op_sel_hi:[1,0]
	v_or_b32_e32 v98, 0x10000, v163
	v_mul_f32_e32 v94, v94, v94
	v_mul_f32_e32 v91, v91, v91
	v_mul_f32_e32 v92, v92, v92
	v_mul_f32_e32 v93, v93, v93
	v_cvt_pk_bf16_f32 v90, v94, v90
	v_pk_mul_f32 v[88:89], v[88:89], v[166:167] op_sel_hi:[1,0]
	v_pk_mul_f32 v[86:87], v[86:87], v[166:167] op_sel_hi:[1,0]
	v_pk_mul_f32 v[84:85], v[84:85], v[166:167] op_sel_hi:[1,0]
	v_max_f32_e32 v82, 0, v82
	v_max_f32_e32 v83, 0, v83
	v_cvt_pk_bf16_f32 v91, v91, v92
	v_cvt_pk_bf16_f32 v92, v99, v95
	v_cvt_pk_bf16_f32 v93, v96, v93
	global_store_dwordx4 v98, v[90:93], s[10:11] nt
	v_max_f32_e32 v86, 0, v86
	v_max_f32_e32 v84, 0, v84
	v_mul_f32_e32 v90, v82, v82
	v_max_f32_e32 v82, 0, v87
	v_mul_f32_e32 v87, v83, v83
	v_max_f32_e32 v83, 0, v88
	v_mul_f32_e32 v86, v86, v86
	v_mul_f32_e32 v82, v82, v82
	v_mul_f32_e32 v83, v83, v83
	v_mul_f32_e32 v88, v84, v84
	v_max_f32_e32 v84, 0, v89
	v_max_f32_e32 v85, 0, v85
	v_mul_f32_e32 v84, v84, v84
	v_mul_f32_e32 v85, v85, v85
	v_cvt_pk_bf16_f32 v82, v86, v82
	v_cvt_pk_bf16_f32 v83, v83, v84
	v_or_b32_e32 v86, 0x10100, v163
	v_cvt_pk_bf16_f32 v84, v90, v87
	v_cvt_pk_bf16_f32 v85, v88, v85
	global_store_dwordx4 v86, v[82:85], s[10:11] nt
	v_pk_mul_f32 v[58:59], v[58:59], v[142:143] op_sel_hi:[1,0]
	v_pk_mul_f32 v[62:63], v[62:63], v[142:143] op_sel_hi:[1,0]
	v_or_b32_e32 v83, 0x18000, v163
	v_mov_b32_e32 v82, v167
	v_pk_mul_f32 v[74:75], v[74:75], v[82:83] op_sel_hi:[1,0]
	v_pk_mul_f32 v[78:79], v[78:79], v[82:83] op_sel_hi:[1,0]
	v_pk_mul_f32 v[76:77], v[76:77], v[82:83] op_sel_hi:[1,0]
	v_max_f32_e32 v74, 0, v74
	v_pk_mul_f32 v[80:81], v[80:81], v[82:83] op_sel_hi:[1,0]
	v_mul_f32_e32 v84, v74, v74
	v_max_f32_e32 v74, 0, v79
	v_max_f32_e32 v75, 0, v75
	v_max_f32_e32 v76, 0, v76
	v_max_f32_e32 v78, 0, v78
	v_mul_f32_e32 v74, v74, v74
	v_mul_f32_e32 v79, v75, v75
	v_max_f32_e32 v75, 0, v80
	v_mul_f32_e32 v80, v76, v76
	v_max_f32_e32 v76, 0, v81
	v_max_f32_e32 v77, 0, v77
	v_pk_mul_f32 v[66:67], v[66:67], v[82:83] op_sel_hi:[1,0]
	v_mul_f32_e32 v78, v78, v78
	v_mul_f32_e32 v75, v75, v75
	v_mul_f32_e32 v76, v76, v76
	v_mul_f32_e32 v77, v77, v77
	v_cvt_pk_bf16_f32 v74, v78, v74
	v_pk_mul_f32 v[72:73], v[72:73], v[82:83] op_sel_hi:[1,0]
	v_pk_mul_f32 v[70:71], v[70:71], v[82:83] op_sel_hi:[1,0]
	v_pk_mul_f32 v[68:69], v[68:69], v[82:83] op_sel_hi:[1,0]
	v_max_f32_e32 v66, 0, v66
	v_max_f32_e32 v67, 0, v67
	v_cvt_pk_bf16_f32 v75, v75, v76
	v_cvt_pk_bf16_f32 v76, v84, v79
	v_cvt_pk_bf16_f32 v77, v80, v77
; #define PG8_GAS __attribute__((address_space(1)))
; #define PG8_PACK8(y0, y1) (u32x4){cvt_pk_bf16((y0)[0], (y0)[1]), cvt_pk_bf16((y0)[2], (y0)[3]), cvt_pk_bf16((y1)[0], (y1)[1]), cvt_pk_bf16((y1)[2], (y1)[3])}
;     __device__ __forceinline__ void operator()(const f32x4 (&acc)[2][2][4][2], const Unit& u, int ui, int wr, int wc, int fr, int fq) const {
;     ...
;         for (int ai = 0; ai < 2; ++ai)
; #pragma unroll
;             for (int m = 0; m < 4; ++m) {
;                 const unsigned row = row0 + ai * HALF + m * 16; const float rs = rsv[ai][m];
; #pragma unroll
;                 for (int bj = 0; bj < 2; ++bj) {
;                     f32x4 y0 = acc[ai][bj][m][0] * rs, y1 = acc[ai][bj][m][1] * rs;
; #pragma unroll
;                     for (int e = 0; e < 4; ++e) { const float a = fmaxf(y0[e], 0.f), b = fmaxf(y1[e], 0.f); y0[e] = a * a; y1[e] = b * b; }
;                     const u32x4 hw = PG8_PACK8(y0, y1);
;     ...
;                     if (probe_mode == 1) { asm volatile("" :: "v"(hw)); } else
;     ...
;                     *(PG8_GAS u32x4*)((PG8_GAS unsigned char*)ws + E_QKVO + (size_t)((unsigned)(u.pm >> 4) * (24u << 20) + (unsigned)(u.pn >> 2) * (8u << 20) + row * 2048u + (colp + bj * HALF) * 2u)) = hw;
	global_store_dwordx4 v83, v[74:77], s[10:11] nt
	v_max_f32_e32 v70, 0, v70
	v_max_f32_e32 v68, 0, v68
	v_mul_f32_e32 v74, v66, v66
	v_max_f32_e32 v66, 0, v71
	v_mul_f32_e32 v71, v67, v67
	v_max_f32_e32 v67, 0, v72
	v_mul_f32_e32 v70, v70, v70
	v_mul_f32_e32 v66, v66, v66
	v_mul_f32_e32 v67, v67, v67
	v_mul_f32_e32 v72, v68, v68
	v_max_f32_e32 v68, 0, v73
	v_max_f32_e32 v69, 0, v69
	v_mul_f32_e32 v68, v68, v68
	v_mul_f32_e32 v69, v69, v69
	v_cvt_pk_bf16_f32 v66, v70, v66
	v_cvt_pk_bf16_f32 v67, v67, v68
	v_or_b32_e32 v70, 0x18100, v163
	v_pk_mul_f32 v[60:61], v[60:61], v[142:143] op_sel_hi:[1,0]
	v_max_f32_e32 v58, 0, v58
	v_cvt_pk_bf16_f32 v68, v74, v71
	v_cvt_pk_bf16_f32 v69, v72, v69
	global_store_dwordx4 v70, v[66:69], s[10:11] nt
	v_pk_mul_f32 v[64:65], v[64:65], v[142:143] op_sel_hi:[1,0]
	v_max_f32_e32 v59, 0, v59
	v_mul_f32_e32 v67, v58, v58
	v_max_f32_e32 v58, 0, v63
	v_max_f32_e32 v60, 0, v60
	v_max_f32_e32 v62, 0, v62
	v_mul_f32_e32 v58, v58, v58
	v_mul_f32_e32 v63, v59, v59
	v_max_f32_e32 v59, 0, v64
	v_mul_f32_e32 v64, v60, v60
	v_max_f32_e32 v60, 0, v65
	v_max_f32_e32 v61, 0, v61
	v_pk_mul_f32 v[50:51], v[50:51], v[142:143] op_sel_hi:[1,0]
	v_add_u32_e32 v66, 0x40000, v163
	v_mul_f32_e32 v62, v62, v62
	v_mul_f32_e32 v59, v59, v59
	v_mul_f32_e32 v60, v60, v60
	v_mul_f32_e32 v61, v61, v61
	v_cvt_pk_bf16_f32 v58, v62, v58
	v_pk_mul_f32 v[56:57], v[56:57], v[142:143] op_sel_hi:[1,0]
	v_pk_mul_f32 v[54:55], v[54:55], v[142:143] op_sel_hi:[1,0]
	v_pk_mul_f32 v[52:53], v[52:53], v[142:143] op_sel_hi:[1,0]
	v_max_f32_e32 v50, 0, v50
	v_max_f32_e32 v51, 0, v51
	v_cvt_pk_bf16_f32 v59, v59, v60
	v_cvt_pk_bf16_f32 v60, v67, v63
	v_cvt_pk_bf16_f32 v61, v64, v61
	global_store_dwordx4 v66, v[58:61], s[10:11] nt
	v_max_f32_e32 v54, 0, v54
	v_max_f32_e32 v52, 0, v52
	v_mul_f32_e32 v58, v50, v50
	v_max_f32_e32 v50, 0, v55
	v_mul_f32_e32 v55, v51, v51
	v_max_f32_e32 v51, 0, v56
	v_mul_f32_e32 v54, v54, v54
	v_mul_f32_e32 v50, v50, v50
	v_mul_f32_e32 v51, v51, v51
	v_mul_f32_e32 v56, v52, v52
	v_max_f32_e32 v52, 0, v57
	v_max_f32_e32 v53, 0, v53
	v_mul_f32_e32 v52, v52, v52
	v_mul_f32_e32 v53, v53, v53
	v_cvt_pk_bf16_f32 v50, v54, v50
	v_cvt_pk_bf16_f32 v51, v51, v52
	v_add_u32_e32 v54, 0x40100, v163
	v_cvt_pk_bf16_f32 v52, v58, v55
	v_cvt_pk_bf16_f32 v53, v56, v53
	global_store_dwordx4 v54, v[50:53], s[10:11] nt
	v_pk_mul_f32 v[26:27], v[26:27], v[140:141] op_sel_hi:[1,0]
	v_pk_mul_f32 v[30:31], v[30:31], v[140:141] op_sel_hi:[1,0]
	v_add_u32_e32 v51, 0x48000, v163
	v_mov_b32_e32 v50, v143
	v_pk_mul_f32 v[42:43], v[42:43], v[50:51] op_sel_hi:[1,0]
	v_pk_mul_f32 v[46:47], v[46:47], v[50:51] op_sel_hi:[1,0]
	v_pk_mul_f32 v[44:45], v[44:45], v[50:51] op_sel_hi:[1,0]
	v_max_f32_e32 v42, 0, v42
	v_pk_mul_f32 v[48:49], v[48:49], v[50:51] op_sel_hi:[1,0]
	v_mul_f32_e32 v52, v42, v42
	v_max_f32_e32 v42, 0, v47
	v_max_f32_e32 v43, 0, v43
	v_max_f32_e32 v44, 0, v44
	v_max_f32_e32 v46, 0, v46
	v_mul_f32_e32 v42, v42, v42
	v_mul_f32_e32 v47, v43, v43
	v_max_f32_e32 v43, 0, v48
	v_mul_f32_e32 v48, v44, v44
	v_max_f32_e32 v44, 0, v49
	v_max_f32_e32 v45, 0, v45
	v_pk_mul_f32 v[34:35], v[34:35], v[50:51] op_sel_hi:[1,0]
	v_mul_f32_e32 v46, v46, v46
	v_mul_f32_e32 v43, v43, v43
	v_mul_f32_e32 v44, v44, v44
	v_mul_f32_e32 v45, v45, v45
	v_cvt_pk_bf16_f32 v42, v46, v42
	v_pk_mul_f32 v[40:41], v[40:41], v[50:51] op_sel_hi:[1,0]
	v_pk_mul_f32 v[38:39], v[38:39], v[50:51] op_sel_hi:[1,0]
	v_pk_mul_f32 v[36:37], v[36:37], v[50:51] op_sel_hi:[1,0]
	v_max_f32_e32 v34, 0, v34
	v_max_f32_e32 v35, 0, v35
	v_cvt_pk_bf16_f32 v43, v43, v44
	v_cvt_pk_bf16_f32 v44, v52, v47
	v_cvt_pk_bf16_f32 v45, v48, v45
	global_store_dwordx4 v51, v[42:45], s[10:11] nt
	v_max_f32_e32 v38, 0, v38
	v_max_f32_e32 v36, 0, v36
	v_mul_f32_e32 v42, v34, v34
	v_max_f32_e32 v34, 0, v39
	v_mul_f32_e32 v39, v35, v35
	v_max_f32_e32 v35, 0, v40
	v_mul_f32_e32 v38, v38, v38
	v_mul_f32_e32 v34, v34, v34
	v_mul_f32_e32 v35, v35, v35
	v_mul_f32_e32 v40, v36, v36
; #define PG8_GAS __attribute__((address_space(1)))
; #define PG8_PACK8(y0, y1) (u32x4){cvt_pk_bf16((y0)[0], (y0)[1]), cvt_pk_bf16((y0)[2], (y0)[3]), cvt_pk_bf16((y1)[0], (y1)[1]), cvt_pk_bf16((y1)[2], (y1)[3])}
; #define PG8_BAR __builtin_amdgcn_s_barrier()
;     __device__ __forceinline__ void operator()(const f32x4 (&acc)[2][2][4][2], const Unit& u, int ui, int wr, int wc, int fr, int fq) const {
;     ...
;         for (int ai = 0; ai < 2; ++ai)
; #pragma unroll
;             for (int m = 0; m < 4; ++m) {
;                 const unsigned row = row0 + ai * HALF + m * 16; const float rs = rsv[ai][m];
; #pragma unroll
;                 for (int bj = 0; bj < 2; ++bj) {
;                     f32x4 y0 = acc[ai][bj][m][0] * rs, y1 = acc[ai][bj][m][1] * rs;
; #pragma unroll
;                     for (int e = 0; e < 4; ++e) { const float a = fmaxf(y0[e], 0.f), b = fmaxf(y1[e], 0.f); y0[e] = a * a; y1[e] = b * b; }
;                     const u32x4 hw = PG8_PACK8(y0, y1);
;     ...
;                     if (probe_mode == 1) { asm volatile("" :: "v"(hw)); } else
;     ...
;                     *(PG8_GAS u32x4*)((PG8_GAS unsigned char*)ws + E_QKVO + (size_t)((unsigned)(u.pm >> 4) * (24u << 20) + (unsigned)(u.pn >> 2) * (8u << 20) + row * 2048u + (colp + bj * HALF) * 2u)) = hw;
; template <class Epi, class Sched, bool ALIGN_EPI = false, bool SP2 = false>
; __device__ __forceinline__ void gemm_phase(PG8_LAS unsigned char* lds, const Gemm g, const Sched& S, const Epi& E, const int tid) {
;     ...
;         if (!has_next) break;
; #pragma unroll
;         for (int a = 0; a < 2; ++a)
; #pragma unroll
;             for (int b = 0; b < 2; ++b)
; #pragma unroll
;                 for (int m = 0; m < 4; ++m)
; #pragma unroll
;                     for (int n = 0; n < 2; ++n) acc[a][b][m][n] = (f32x4){0.f, 0.f, 0.f, 0.f};
;         cur = nxt; cA = nA; cB = nB; ++ui;
;         if constexpr (ALIGN_EPI) { if (wr == 1) PG8_BAR; }
;     }
	v_max_f32_e32 v36, 0, v41
	v_max_f32_e32 v37, 0, v37
	v_mul_f32_e32 v36, v36, v36
	v_mul_f32_e32 v37, v37, v37
	v_cvt_pk_bf16_f32 v34, v38, v34
	v_cvt_pk_bf16_f32 v35, v35, v36
	v_add_u32_e32 v38, 0x48100, v163
	v_pk_mul_f32 v[28:29], v[28:29], v[140:141] op_sel_hi:[1,0]
	v_max_f32_e32 v26, 0, v26
	v_cvt_pk_bf16_f32 v36, v42, v39
	v_cvt_pk_bf16_f32 v37, v40, v37
	global_store_dwordx4 v38, v[34:37], s[10:11] nt
	v_pk_mul_f32 v[32:33], v[32:33], v[140:141] op_sel_hi:[1,0]
	v_max_f32_e32 v27, 0, v27
	v_mul_f32_e32 v35, v26, v26
	v_max_f32_e32 v26, 0, v31
	v_max_f32_e32 v28, 0, v28
	v_max_f32_e32 v30, 0, v30
	v_mul_f32_e32 v26, v26, v26
	v_mul_f32_e32 v31, v27, v27
	v_max_f32_e32 v27, 0, v32
	v_mul_f32_e32 v32, v28, v28
	v_max_f32_e32 v28, 0, v33
	v_max_f32_e32 v29, 0, v29
	v_pk_mul_f32 v[18:19], v[18:19], v[140:141] op_sel_hi:[1,0]
	v_add_u32_e32 v34, 0x50000, v163
	v_mul_f32_e32 v30, v30, v30
	v_mul_f32_e32 v27, v27, v27
	v_mul_f32_e32 v28, v28, v28
	v_mul_f32_e32 v29, v29, v29
	v_cvt_pk_bf16_f32 v26, v30, v26
	v_pk_mul_f32 v[24:25], v[24:25], v[140:141] op_sel_hi:[1,0]
	v_pk_mul_f32 v[22:23], v[22:23], v[140:141] op_sel_hi:[1,0]
	v_pk_mul_f32 v[20:21], v[20:21], v[140:141] op_sel_hi:[1,0]
	v_max_f32_e32 v18, 0, v18
	v_max_f32_e32 v19, 0, v19
	v_cvt_pk_bf16_f32 v27, v27, v28
	v_cvt_pk_bf16_f32 v28, v35, v31
	v_cvt_pk_bf16_f32 v29, v32, v29
	global_store_dwordx4 v34, v[26:29], s[10:11] nt
	v_max_f32_e32 v22, 0, v22
	v_max_f32_e32 v20, 0, v20
	v_mul_f32_e32 v26, v18, v18
	v_max_f32_e32 v18, 0, v23
	v_mul_f32_e32 v23, v19, v19
	v_max_f32_e32 v19, 0, v24
	v_mul_f32_e32 v22, v22, v22
	v_mul_f32_e32 v18, v18, v18
	v_mul_f32_e32 v19, v19, v19
	v_mul_f32_e32 v24, v20, v20
	v_max_f32_e32 v20, 0, v25
	v_max_f32_e32 v21, 0, v21
	v_mul_f32_e32 v20, v20, v20
	v_mul_f32_e32 v21, v21, v21
	v_cvt_pk_bf16_f32 v18, v22, v18
	v_cvt_pk_bf16_f32 v19, v19, v20
	v_add_u32_e32 v22, 0x50100, v163
	v_cvt_pk_bf16_f32 v20, v26, v23
	v_cvt_pk_bf16_f32 v21, v24, v21
	global_store_dwordx4 v22, v[18:21], s[10:11] nt
	s_andn2_b64 vcc, exec, s[0:1]
	s_mov_b64 s[0:1], -1
	v_add_u32_e32 v19, 0x58000, v163
	v_mov_b32_e32 v18, v141
	v_pk_mul_f32 v[10:11], v[10:11], v[18:19] op_sel_hi:[1,0]
	v_pk_mul_f32 v[14:15], v[14:15], v[18:19] op_sel_hi:[1,0]
	v_pk_mul_f32 v[12:13], v[12:13], v[18:19] op_sel_hi:[1,0]
	v_max_f32_e32 v10, 0, v10
	v_pk_mul_f32 v[16:17], v[16:17], v[18:19] op_sel_hi:[1,0]
	v_mul_f32_e32 v20, v10, v10
	v_max_f32_e32 v10, 0, v15
	v_max_f32_e32 v11, 0, v11
	v_max_f32_e32 v12, 0, v12
	v_max_f32_e32 v14, 0, v14
	v_mul_f32_e32 v10, v10, v10
	v_mul_f32_e32 v15, v11, v11
	v_max_f32_e32 v11, 0, v16
	v_mul_f32_e32 v16, v12, v12
	v_max_f32_e32 v12, 0, v17
	v_max_f32_e32 v13, 0, v13
	v_pk_mul_f32 v[2:3], v[2:3], v[18:19] op_sel_hi:[1,0]
	v_mul_f32_e32 v14, v14, v14
	v_mul_f32_e32 v11, v11, v11
	v_mul_f32_e32 v12, v12, v12
	v_mul_f32_e32 v13, v13, v13
	v_cvt_pk_bf16_f32 v10, v14, v10
	v_pk_mul_f32 v[6:7], v[6:7], v[18:19] op_sel_hi:[1,0]
	v_pk_mul_f32 v[4:5], v[4:5], v[18:19] op_sel_hi:[1,0]
	v_max_f32_e32 v2, 0, v2
	v_cvt_pk_bf16_f32 v11, v11, v12
	v_cvt_pk_bf16_f32 v12, v20, v15
	v_cvt_pk_bf16_f32 v13, v16, v13
	global_store_dwordx4 v19, v[10:13], s[10:11] nt
	v_pk_mul_f32 v[8:9], v[8:9], v[18:19] op_sel_hi:[1,0]
	v_max_f32_e32 v6, 0, v6
	v_mul_f32_e32 v10, v2, v2
	v_max_f32_e32 v2, 0, v7
	v_max_f32_e32 v3, 0, v3
	v_max_f32_e32 v4, 0, v4
	v_mul_f32_e32 v6, v6, v6
	v_mul_f32_e32 v2, v2, v2
	v_mul_f32_e32 v7, v3, v3
	v_max_f32_e32 v3, 0, v8
	v_mul_f32_e32 v8, v4, v4
	v_max_f32_e32 v4, 0, v9
	v_max_f32_e32 v5, 0, v5
	v_mul_f32_e32 v3, v3, v3
	v_mul_f32_e32 v4, v4, v4
	v_mul_f32_e32 v5, v5, v5
	v_cvt_pk_bf16_f32 v2, v6, v2
	v_add_u32_e32 v6, 0x58100, v163
	v_cvt_pk_bf16_f32 v3, v3, v4
	v_cvt_pk_bf16_f32 v4, v10, v7
	v_cvt_pk_bf16_f32 v5, v8, v5
	global_store_dwordx4 v6, v[2:5], s[10:11] nt
	s_mov_b32 s100, 2
	s_cbranch_vccnz .LBB0_53
	s_andn2_b64 vcc, exec, s[6:7]
	s_cbranch_vccnz .LBB0_52
	s_barrier
	s_branch .LBB0_52
